# v39 + P8 epilogue per-word waits removed + hand-written P4 epilogue + balanced saddr DMA in the bf16 score GEMM loop
# speedup vs baseline: 1.0220x; 1.0220x over previous
.LBB0_687:
	s_add_u32 s72, s24, 0xfff00000
	s_addc_u32 s73, s25, -1
	s_mov_b32 m0, s44
	s_nop 0
	global_load_lds_dwordx4 v128, s[72:73]
	s_mov_b32 m0, s45
	s_nop 0
	global_load_lds_dwordx4 v130, s[72:73]
	ds_read_b128 v[160:163], v142
	ds_read_b128 v[164:167], v143
	ds_read_b128 v[168:171], v144
	ds_read_b128 v[172:175], v145
	ds_read_b128 v[176:179], v146
	ds_read_b128 v[180:183], v147
	ds_read_b128 v[184:187], v148
	ds_read_b128 v[188:191], v149
	s_add_u32 s26, s24, 0xfff00080
	s_addc_u32 s27, s25, -1
	s_cmp_eq_u32 s54, 60
	s_cselect_b32 s29, s19, s27
	s_cselect_b32 s28, s50, s26
	s_cselect_b32 s27, s17, s53
	s_cselect_b32 s26, s51, s52
	s_add_i32 m0, s33, 0xc000
	ds_read_b128 v[192:195], v158
	ds_read_b128 v[196:199], v158 offset:1024
	ds_read_b128 v[200:203], v158 offset:2048
	ds_read_b128 v[204:207], v158 offset:3072
	ds_read_b128 v[208:211], v158 offset:4096
	ds_read_b128 v[212:215], v158 offset:5120
	ds_read_b128 v[216:219], v158 offset:6144
	ds_read_b128 v[220:223], v158 offset:7168
	global_load_lds_dwordx4 v134, s[24:25]
	s_add_i32 m0, s33, 0xe000
	s_nop 0
	global_load_lds_dwordx4 v136, s[24:25]
	s_waitcnt vmcnt(8)
	s_waitcnt lgkmcnt(0)
	s_barrier
	s_setprio 1
	s_waitcnt lgkmcnt(0)
	v_mfma_f32_16x16x32_bf16 v[124:127], v[160:163], v[192:195], v[124:127]
	v_mfma_f32_16x16x32_bf16 v[120:123], v[168:171], v[192:195], v[120:123]
	v_mfma_f32_16x16x32_bf16 v[116:119], v[160:163], v[200:203], v[116:119]
	v_mfma_f32_16x16x32_bf16 v[112:115], v[168:171], v[200:203], v[112:115]
	v_mfma_f32_16x16x32_bf16 v[108:111], v[160:163], v[208:211], v[108:111]
	v_mfma_f32_16x16x32_bf16 v[104:107], v[168:171], v[208:211], v[104:107]
	v_mfma_f32_16x16x32_bf16 v[100:103], v[160:163], v[216:219], v[100:103]
	v_mfma_f32_16x16x32_bf16 v[96:99], v[168:171], v[216:219], v[96:99]
	v_mfma_f32_16x16x32_bf16 v[124:127], v[164:167], v[196:199], v[124:127]
	v_mfma_f32_16x16x32_bf16 v[120:123], v[172:175], v[196:199], v[120:123]
	v_mfma_f32_16x16x32_bf16 v[116:119], v[164:167], v[204:207], v[116:119]
	v_mfma_f32_16x16x32_bf16 v[112:115], v[172:175], v[204:207], v[112:115]
	v_mfma_f32_16x16x32_bf16 v[108:111], v[164:167], v[212:215], v[108:111]
	v_mfma_f32_16x16x32_bf16 v[104:107], v[172:175], v[212:215], v[104:107]
	v_mfma_f32_16x16x32_bf16 v[100:103], v[164:167], v[220:223], v[100:103]
	v_mfma_f32_16x16x32_bf16 v[96:99], v[172:175], v[220:223], v[96:99]
	s_setprio 0
	s_setprio 1
	v_mfma_f32_16x16x32_bf16 v[92:95], v[176:179], v[192:195], v[92:95]
	v_mfma_f32_16x16x32_bf16 v[88:91], v[184:187], v[192:195], v[88:91]
	v_mfma_f32_16x16x32_bf16 v[84:87], v[176:179], v[200:203], v[84:87]
	v_mfma_f32_16x16x32_bf16 v[80:83], v[184:187], v[200:203], v[80:83]
	v_mfma_f32_16x16x32_bf16 v[76:79], v[176:179], v[208:211], v[76:79]
	v_mfma_f32_16x16x32_bf16 v[72:75], v[184:187], v[208:211], v[72:75]
	v_mfma_f32_16x16x32_bf16 v[68:71], v[176:179], v[216:219], v[68:71]
	v_mfma_f32_16x16x32_bf16 v[64:67], v[184:187], v[216:219], v[64:67]
	v_mfma_f32_16x16x32_bf16 v[92:95], v[180:183], v[196:199], v[92:95]
	v_mfma_f32_16x16x32_bf16 v[88:91], v[188:191], v[196:199], v[88:91]
	v_mfma_f32_16x16x32_bf16 v[84:87], v[180:183], v[204:207], v[84:87]
	v_mfma_f32_16x16x32_bf16 v[80:83], v[188:191], v[204:207], v[80:83]
	v_mfma_f32_16x16x32_bf16 v[76:79], v[180:183], v[212:215], v[76:79]
	v_mfma_f32_16x16x32_bf16 v[72:75], v[188:191], v[212:215], v[72:75]
	v_mfma_f32_16x16x32_bf16 v[68:71], v[180:183], v[220:223], v[68:71]
	v_mfma_f32_16x16x32_bf16 v[64:67], v[188:191], v[220:223], v[64:67]
	s_setprio 0
	s_barrier
	s_mov_b32 m0, s34
	v_lshl_add_u64 v[224:225], s[26:27], 0, v[128:129]
	s_add_u32 s56, s26, 0x100000
	ds_read_b128 v[192:195], v158 offset:16384
	ds_read_b128 v[196:199], v158 offset:17408
	ds_read_b128 v[200:203], v158 offset:18432
	ds_read_b128 v[204:207], v158 offset:19456
	ds_read_b128 v[208:211], v158 offset:20480
	ds_read_b128 v[212:215], v158 offset:21504
	ds_read_b128 v[216:219], v158 offset:22528
	ds_read_b128 v[220:223], v158 offset:23552
	global_load_lds_dwordx4 v[224:225], off
	v_lshl_add_u64 v[226:227], s[26:27], 0, v[130:131]
	s_mov_b32 m0, s35
	s_addc_u32 s57, s27, 0
	global_load_lds_dwordx4 v[226:227], off
	s_mov_b32 m0, s36
	s_nop 0
	global_load_lds_dwordx4 v128, s[56:57]
	s_mov_b32 m0, s37
	s_nop 0
	global_load_lds_dwordx4 v130, s[56:57]
	s_waitcnt vmcnt(6)
	s_waitcnt lgkmcnt(0)
	s_barrier
	s_setprio 1
	s_waitcnt lgkmcnt(0)
	v_mfma_f32_16x16x32_bf16 v[60:63], v[160:163], v[192:195], v[60:63]
	v_mfma_f32_16x16x32_bf16 v[56:59], v[168:171], v[192:195], v[56:59]
	v_mfma_f32_16x16x32_bf16 v[52:55], v[160:163], v[200:203], v[52:55]
	v_mfma_f32_16x16x32_bf16 v[48:51], v[168:171], v[200:203], v[48:51]
	v_mfma_f32_16x16x32_bf16 v[44:47], v[160:163], v[208:211], v[44:47]
	v_mfma_f32_16x16x32_bf16 v[40:43], v[168:171], v[208:211], v[40:43]
	v_mfma_f32_16x16x32_bf16 v[36:39], v[160:163], v[216:219], v[36:39]
	v_mfma_f32_16x16x32_bf16 v[32:35], v[168:171], v[216:219], v[32:35]
	v_mfma_f32_16x16x32_bf16 v[60:63], v[164:167], v[196:199], v[60:63]
	v_mfma_f32_16x16x32_bf16 v[56:59], v[172:175], v[196:199], v[56:59]
	v_mfma_f32_16x16x32_bf16 v[52:55], v[164:167], v[204:207], v[52:55]
	v_mfma_f32_16x16x32_bf16 v[48:51], v[172:175], v[204:207], v[48:51]
	v_mfma_f32_16x16x32_bf16 v[44:47], v[164:167], v[212:215], v[44:47]
	v_mfma_f32_16x16x32_bf16 v[40:43], v[172:175], v[212:215], v[40:43]
	v_mfma_f32_16x16x32_bf16 v[36:39], v[164:167], v[220:223], v[36:39]
	v_mfma_f32_16x16x32_bf16 v[32:35], v[172:175], v[220:223], v[32:35]
	s_setprio 0
	s_setprio 1
	v_mfma_f32_16x16x32_bf16 v[28:31], v[176:179], v[192:195], v[28:31]
	v_mfma_f32_16x16x32_bf16 v[24:27], v[184:187], v[192:195], v[24:27]
	v_mfma_f32_16x16x32_bf16 v[20:23], v[176:179], v[200:203], v[20:23]
	v_mfma_f32_16x16x32_bf16 v[16:19], v[184:187], v[200:203], v[16:19]
	v_mfma_f32_16x16x32_bf16 v[12:15], v[176:179], v[208:211], v[12:15]
	v_mfma_f32_16x16x32_bf16 v[8:11], v[184:187], v[208:211], v[8:11]
	v_mfma_f32_16x16x32_bf16 v[4:7], v[176:179], v[216:219], v[4:7]
	v_mfma_f32_16x16x32_bf16 v[0:3], v[184:187], v[216:219], v[0:3]
	v_mfma_f32_16x16x32_bf16 v[28:31], v[180:183], v[196:199], v[28:31]
	v_mfma_f32_16x16x32_bf16 v[24:27], v[188:191], v[196:199], v[24:27]
	v_mfma_f32_16x16x32_bf16 v[20:23], v[180:183], v[204:207], v[20:23]
	v_mfma_f32_16x16x32_bf16 v[16:19], v[188:191], v[204:207], v[16:19]
	v_mfma_f32_16x16x32_bf16 v[12:15], v[180:183], v[212:215], v[12:15]
	v_mfma_f32_16x16x32_bf16 v[8:11], v[188:191], v[212:215], v[8:11]
	v_mfma_f32_16x16x32_bf16 v[4:7], v[180:183], v[220:223], v[4:7]
	v_mfma_f32_16x16x32_bf16 v[0:3], v[188:191], v[220:223], v[0:3]
	s_setprio 0
	s_barrier
	s_mov_b32 m0, s33
	s_nop 0
	global_load_lds_dwordx4 v128, s[28:29]
	s_mov_b32 m0, s38
	s_nop 0
	global_load_lds_dwordx4 v130, s[28:29]
	ds_read_b128 v[160:163], v150
	ds_read_b128 v[164:167], v151
	ds_read_b128 v[168:171], v152
	ds_read_b128 v[172:175], v153
	ds_read_b128 v[176:179], v154
	ds_read_b128 v[180:183], v155
	ds_read_b128 v[184:187], v156
	ds_read_b128 v[188:191], v157
	s_add_u32 s28, s28, 0x100000
	s_addc_u32 s29, s29, 0
	s_mov_b32 m0, s39
	ds_read_b128 v[192:195], v158 offset:32768
	ds_read_b128 v[196:199], v158 offset:33792
	ds_read_b128 v[200:203], v158 offset:34816
	ds_read_b128 v[204:207], v158 offset:35840
	ds_read_b128 v[208:211], v158 offset:36864
	ds_read_b128 v[212:215], v158 offset:37888
	ds_read_b128 v[216:219], v158 offset:38912
	ds_read_b128 v[220:223], v158 offset:39936
	global_load_lds_dwordx4 v128, s[28:29]
	s_mov_b32 m0, s40
	s_nop 0
	global_load_lds_dwordx4 v130, s[28:29]
	s_waitcnt vmcnt(8)
	s_waitcnt lgkmcnt(0)
	s_barrier
	s_setprio 1
	s_waitcnt lgkmcnt(0)
	v_mfma_f32_16x16x32_bf16 v[124:127], v[160:163], v[192:195], v[124:127]
	v_mfma_f32_16x16x32_bf16 v[120:123], v[168:171], v[192:195], v[120:123]
	v_mfma_f32_16x16x32_bf16 v[116:119], v[160:163], v[200:203], v[116:119]
	v_mfma_f32_16x16x32_bf16 v[112:115], v[168:171], v[200:203], v[112:115]
	v_mfma_f32_16x16x32_bf16 v[108:111], v[160:163], v[208:211], v[108:111]
	v_mfma_f32_16x16x32_bf16 v[104:107], v[168:171], v[208:211], v[104:107]
	v_mfma_f32_16x16x32_bf16 v[100:103], v[160:163], v[216:219], v[100:103]
	v_mfma_f32_16x16x32_bf16 v[96:99], v[168:171], v[216:219], v[96:99]
	v_mfma_f32_16x16x32_bf16 v[124:127], v[164:167], v[196:199], v[124:127]
	v_mfma_f32_16x16x32_bf16 v[120:123], v[172:175], v[196:199], v[120:123]
	v_mfma_f32_16x16x32_bf16 v[116:119], v[164:167], v[204:207], v[116:119]
	v_mfma_f32_16x16x32_bf16 v[112:115], v[172:175], v[204:207], v[112:115]
	v_mfma_f32_16x16x32_bf16 v[108:111], v[164:167], v[212:215], v[108:111]
	v_mfma_f32_16x16x32_bf16 v[104:107], v[172:175], v[212:215], v[104:107]
	v_mfma_f32_16x16x32_bf16 v[100:103], v[164:167], v[220:223], v[100:103]
	v_mfma_f32_16x16x32_bf16 v[96:99], v[172:175], v[220:223], v[96:99]
	s_setprio 0
	s_setprio 1
	v_mfma_f32_16x16x32_bf16 v[92:95], v[176:179], v[192:195], v[92:95]
	v_mfma_f32_16x16x32_bf16 v[88:91], v[184:187], v[192:195], v[88:91]
	v_mfma_f32_16x16x32_bf16 v[84:87], v[176:179], v[200:203], v[84:87]
	v_mfma_f32_16x16x32_bf16 v[80:83], v[184:187], v[200:203], v[80:83]
	v_mfma_f32_16x16x32_bf16 v[76:79], v[176:179], v[208:211], v[76:79]
	v_mfma_f32_16x16x32_bf16 v[72:75], v[184:187], v[208:211], v[72:75]
	v_mfma_f32_16x16x32_bf16 v[68:71], v[176:179], v[216:219], v[68:71]
	v_mfma_f32_16x16x32_bf16 v[64:67], v[184:187], v[216:219], v[64:67]
	v_mfma_f32_16x16x32_bf16 v[92:95], v[180:183], v[196:199], v[92:95]
	v_mfma_f32_16x16x32_bf16 v[88:91], v[188:191], v[196:199], v[88:91]
	v_mfma_f32_16x16x32_bf16 v[84:87], v[180:183], v[204:207], v[84:87]
	v_mfma_f32_16x16x32_bf16 v[80:83], v[188:191], v[204:207], v[80:83]
	v_mfma_f32_16x16x32_bf16 v[76:79], v[180:183], v[212:215], v[76:79]
	v_mfma_f32_16x16x32_bf16 v[72:75], v[188:191], v[212:215], v[72:75]
	v_mfma_f32_16x16x32_bf16 v[68:71], v[180:183], v[220:223], v[68:71]
	v_mfma_f32_16x16x32_bf16 v[64:67], v[188:191], v[220:223], v[64:67]
	s_setprio 0
	s_barrier
	s_mov_b32 m0, s42
	v_lshl_add_u64 v[224:225], v[224:225], 0, s[10:11]
	s_add_u32 s26, s26, 0x100080
	ds_read_b128 v[192:195], v158 offset:49152
	ds_read_b128 v[196:199], v158 offset:50176
	ds_read_b128 v[200:203], v158 offset:51200
	ds_read_b128 v[204:207], v158 offset:52224
	ds_read_b128 v[208:211], v158 offset:53248
	ds_read_b128 v[212:215], v158 offset:54272
	ds_read_b128 v[216:219], v158 offset:55296
	ds_read_b128 v[220:223], v158 offset:56320
	global_load_lds_dwordx4 v[224:225], off
	v_lshl_add_u64 v[224:225], v[226:227], 0, s[10:11]
	s_mov_b32 m0, s43
	s_addc_u32 s27, s27, 0
	global_load_lds_dwordx4 v[224:225], off
	s_mov_b32 m0, s46
	s_nop 0
	global_load_lds_dwordx4 v128, s[26:27]
	s_mov_b32 m0, s47
	s_nop 0
	global_load_lds_dwordx4 v130, s[26:27]
	s_waitcnt vmcnt(6)
	s_waitcnt lgkmcnt(0)
	s_barrier
	s_setprio 1
	s_waitcnt lgkmcnt(0)
	v_mfma_f32_16x16x32_bf16 v[60:63], v[160:163], v[192:195], v[60:63]
	v_mfma_f32_16x16x32_bf16 v[56:59], v[168:171], v[192:195], v[56:59]
	v_mfma_f32_16x16x32_bf16 v[52:55], v[160:163], v[200:203], v[52:55]
	v_mfma_f32_16x16x32_bf16 v[48:51], v[168:171], v[200:203], v[48:51]
	v_mfma_f32_16x16x32_bf16 v[44:47], v[160:163], v[208:211], v[44:47]
	v_mfma_f32_16x16x32_bf16 v[40:43], v[168:171], v[208:211], v[40:43]
	v_mfma_f32_16x16x32_bf16 v[36:39], v[160:163], v[216:219], v[36:39]
	v_mfma_f32_16x16x32_bf16 v[32:35], v[168:171], v[216:219], v[32:35]
	v_mfma_f32_16x16x32_bf16 v[60:63], v[164:167], v[196:199], v[60:63]
	v_mfma_f32_16x16x32_bf16 v[56:59], v[172:175], v[196:199], v[56:59]
	v_mfma_f32_16x16x32_bf16 v[52:55], v[164:167], v[204:207], v[52:55]
	v_mfma_f32_16x16x32_bf16 v[48:51], v[172:175], v[204:207], v[48:51]
	v_mfma_f32_16x16x32_bf16 v[44:47], v[164:167], v[212:215], v[44:47]
	v_mfma_f32_16x16x32_bf16 v[40:43], v[172:175], v[212:215], v[40:43]
	v_mfma_f32_16x16x32_bf16 v[36:39], v[164:167], v[220:223], v[36:39]
	v_mfma_f32_16x16x32_bf16 v[32:35], v[172:175], v[220:223], v[32:35]
	s_setprio 0
	s_setprio 1
	v_mfma_f32_16x16x32_bf16 v[28:31], v[176:179], v[192:195], v[28:31]
	v_mfma_f32_16x16x32_bf16 v[24:27], v[184:187], v[192:195], v[24:27]
	v_mfma_f32_16x16x32_bf16 v[20:23], v[176:179], v[200:203], v[20:23]
	v_mfma_f32_16x16x32_bf16 v[16:19], v[184:187], v[200:203], v[16:19]
	v_mfma_f32_16x16x32_bf16 v[12:15], v[176:179], v[208:211], v[12:15]
	v_mfma_f32_16x16x32_bf16 v[8:11], v[184:187], v[208:211], v[8:11]
	v_mfma_f32_16x16x32_bf16 v[4:7], v[176:179], v[216:219], v[4:7]
	v_mfma_f32_16x16x32_bf16 v[0:3], v[184:187], v[216:219], v[0:3]
	v_mfma_f32_16x16x32_bf16 v[28:31], v[180:183], v[196:199], v[28:31]
	v_mfma_f32_16x16x32_bf16 v[24:27], v[188:191], v[196:199], v[24:27]
	v_mfma_f32_16x16x32_bf16 v[20:23], v[180:183], v[204:207], v[20:23]
	v_mfma_f32_16x16x32_bf16 v[16:19], v[188:191], v[204:207], v[16:19]
	v_mfma_f32_16x16x32_bf16 v[12:15], v[180:183], v[212:215], v[12:15]
	v_mfma_f32_16x16x32_bf16 v[8:11], v[188:191], v[212:215], v[8:11]
	v_mfma_f32_16x16x32_bf16 v[4:7], v[180:183], v[220:223], v[4:7]
	v_mfma_f32_16x16x32_bf16 v[0:3], v[188:191], v[220:223], v[0:3]
	s_setprio 0
	s_barrier
	s_add_i32 s54, s54, 2
	s_add_u32 s24, s24, 0x100
	s_addc_u32 s25, s25, 0
	s_add_u32 s52, s52, 0x100
	s_addc_u32 s53, s53, 0
	s_cmp_gt_u32 s54, 61
	s_cbranch_scc0 .LBB0_687
	s_and_b64 vcc, exec, s[12:13]
	s_cbranch_vccz .LBB0_690
	s_barrier
